# v55 + the 20 s_nop 0 after LDS waits in the attention QK phases removed
# baseline (speedup 1.0000x reference)
; template <int OFF> __device__ __forceinline__ bf16x8 k_read(int kb) { bf16x8 r; asm volatile("ds_read_b128 %0, %1 offset:%2" : "=&v"(r) : "v"(kb), "i"(OFF) : "memory"); return r; }
; #define QK_STEP(D, X, Y, NEXT, N) do { K_WAIT(N, X, Y); \
;         p0 = __builtin_amdgcn_mfma_f32_32x32x16_bf16(X, qr[D], p0, 0, 0, 0); p1 = __builtin_amdgcn_mfma_f32_32x32x16_bf16(Y, qr[D], p1, 0, 0, 0); \
;         if constexpr ((NEXT) < 12) { X = k_read<(NEXT) * 32>(kb); Y = k_read<R1 + (NEXT) * 32>(kb); } } while (0)
; __device__ __forceinline__ void partialSM(f32x16& p0, f32x16& p1, float& m_reg, float& mn, float& alpha) {
;     constexpr float C = SCALE * 1.4426950408889634f;
;     float pmax = p0[0];
; #pragma unroll
;     for (int r = 1; r < 16; ++r) pmax = fmaxf(pmax, p0[r]);
; #pragma unroll
;     for (int r = 0; r < 16; ++r) pmax = fmaxf(pmax, p1[r]);
;     { auto rr = __builtin_amdgcn_permlane32_swap(__float_as_uint(pmax), __float_as_uint(pmax), false, false);
;       pmax = fmaxf(__uint_as_float(rr[0]), __uint_as_float(rr[1])); }
;     if (__builtin_expect(__all(pmax - m_reg <= THR / SCALE), 1)) { mn = m_reg; alpha = 1.f; }
;     else { mn = fmaxf(m_reg, pmax); alpha = __builtin_amdgcn_exp2f((m_reg - mn) * C); m_reg = mn; }
; __device__ __forceinline__ void qkt(f32x16& p0, f32x16& p1, const unsigned char* Ks, const bf16x8* qr, int r32, int hi) {
;     const int kb = (int)(uintptr_t)Ks + r32 * KPITCH + hi * 16;
;     constexpr int R1 = 32 * KPITCH;
;     p0 = f32x16{}; p1 = f32x16{};
;     bf16x8 a0 = k_read<0>(kb), a1 = k_read<R1>(kb), a2 = k_read<32>(kb), a3 = k_read<R1 + 32>(kb), a4 = k_read<64>(kb), a5 = k_read<R1 + 64>(kb);
;     ...
;     QK_STEP(0, a0, a1, 3, 4); QK_STEP(1, a2, a3, 4, 4); QK_STEP(2, a4, a5, 5, 4);
;     QK_STEP(3, a0, a1, 6, 4); QK_STEP(4, a2, a3, 7, 4); QK_STEP(5, a4, a5, 8, 4);
;     QK_STEP(6, a0, a1, 9, 4); QK_STEP(7, a2, a3, 10, 4); QK_STEP(8, a4, a5, 11, 4);
;     QK_STEP(9, a0, a1, 12, 4); QK_STEP(10, a2, a3, 12, 2); QK_STEP(11, a4, a5, 12, 0);
.LBB0_1001:
	s_bitcmp1_b32 s0, 0
	s_cselect_b32 s49, 0x6400, 0
	s_cmp_lg_u32 0, -1
	s_cselect_b32 s0, 0, 0
	s_add_i32 s0, s0, s49
	v_add_u32_e32 v174, s0, v178
	ds_read_b128 v[64:67], v174 offset:0
	ds_read_b128 v[68:71], v174 offset:0x3200
	ds_read_b128 v[180:183], v174 offset:32
	ds_read_b128 v[184:187], v174 offset:0x3220
	ds_read_b128 v[188:191], v174 offset:64
	ds_read_b128 v[192:195], v174 offset:0x3240
	s_waitcnt lgkmcnt(4)
	ds_read_b128 v[196:199], v174 offset:0x60
	ds_read_b128 v[200:203], v174 offset:0x3260
	s_waitcnt lgkmcnt(4)
	v_mfma_f32_32x32x16_bf16 v[80:95], v[64:67], v[142:145], 0
	v_mfma_f32_32x32x16_bf16 v[64:79], v[68:71], v[142:145], 0
	v_mfma_f32_32x32x16_bf16 v[80:95], v[180:183], v[138:141], v[80:95]
	ds_read_b128 v[180:183], v174 offset:0x80
	v_mfma_f32_32x32x16_bf16 v[64:79], v[184:187], v[138:141], v[64:79]
	ds_read_b128 v[184:187], v174 offset:0x3280
	s_waitcnt lgkmcnt(4)
	v_mfma_f32_32x32x16_bf16 v[80:95], v[188:191], v[134:137], v[80:95]
	ds_read_b128 v[188:191], v174 offset:0xa0
	v_mfma_f32_32x32x16_bf16 v[64:79], v[192:195], v[134:137], v[64:79]
	ds_read_b128 v[192:195], v174 offset:0x32a0
	s_waitcnt lgkmcnt(4)
	v_mfma_f32_32x32x16_bf16 v[80:95], v[196:199], v[130:133], v[80:95]
	ds_read_b128 v[196:199], v174 offset:0xc0
	v_mfma_f32_32x32x16_bf16 v[64:79], v[200:203], v[130:133], v[64:79]
	ds_read_b128 v[200:203], v174 offset:0x32c0
	s_waitcnt lgkmcnt(4)
	v_mfma_f32_32x32x16_bf16 v[80:95], v[180:183], v[126:129], v[80:95]
	ds_read_b128 v[180:183], v174 offset:0xe0
	v_mfma_f32_32x32x16_bf16 v[64:79], v[184:187], v[126:129], v[64:79]
	ds_read_b128 v[184:187], v174 offset:0x32e0
	s_waitcnt lgkmcnt(4)
	v_mfma_f32_32x32x16_bf16 v[80:95], v[188:191], v[122:125], v[80:95]
	ds_read_b128 v[188:191], v174 offset:0x100
	v_mfma_f32_32x32x16_bf16 v[64:79], v[192:195], v[122:125], v[64:79]
	ds_read_b128 v[192:195], v174 offset:0x3300
	s_waitcnt lgkmcnt(4)
	v_mfma_f32_32x32x16_bf16 v[80:95], v[196:199], v[118:121], v[80:95]
	ds_read_b128 v[196:199], v174 offset:0x120
	v_mfma_f32_32x32x16_bf16 v[64:79], v[200:203], v[118:121], v[64:79]
	ds_read_b128 v[200:203], v174 offset:0x3320
	s_waitcnt lgkmcnt(4)
	v_mfma_f32_32x32x16_bf16 v[80:95], v[180:183], v[114:117], v[80:95]
	ds_read_b128 v[180:183], v174 offset:0x140
	v_mfma_f32_32x32x16_bf16 v[64:79], v[184:187], v[114:117], v[64:79]
	ds_read_b128 v[184:187], v174 offset:0x3340
	s_waitcnt lgkmcnt(4)
	v_mfma_f32_32x32x16_bf16 v[80:95], v[188:191], v[110:113], v[80:95]
	ds_read_b128 v[188:191], v174 offset:0x160
	v_mfma_f32_32x32x16_bf16 v[64:79], v[192:195], v[110:113], v[64:79]
	ds_read_b128 v[192:195], v174 offset:0x3360
	s_waitcnt lgkmcnt(4)
	s_waitcnt lgkmcnt(2)
	s_waitcnt lgkmcnt(0)
	v_add_u32_e32 v207, s49, v172
	ds_read_b64_tr_b16 v[220:221], v207 offset:0
	ds_read_b64_tr_b16 v[222:223], v207 offset:1600
	ds_read_b64_tr_b16 v[224:225], v207 offset:64
	ds_read_b64_tr_b16 v[226:227], v207 offset:1664
	ds_read_b64_tr_b16 v[228:229], v207 offset:128
	ds_read_b64_tr_b16 v[230:231], v207 offset:1728
	ds_read_b64_tr_b16 v[232:233], v207 offset:192
	ds_read_b64_tr_b16 v[234:235], v207 offset:1792
	ds_read_b64_tr_b16 v[236:237], v207 offset:6400
	ds_read_b64_tr_b16 v[238:239], v207 offset:8000
	ds_read_b64_tr_b16 v[240:241], v207 offset:6464
	ds_read_b64_tr_b16 v[242:243], v207 offset:8064
	ds_read_b64_tr_b16 v[244:245], v207 offset:6528
	ds_read_b64_tr_b16 v[246:247], v207 offset:8128
	ds_read_b64_tr_b16 v[248:249], v207 offset:6592
	ds_read_b64_tr_b16 v[250:251], v207 offset:8192
	v_mfma_f32_32x32x16_bf16 v[80:95], v[196:199], v[106:109], v[80:95]
	v_mfma_f32_32x32x16_bf16 v[80:95], v[180:183], v[102:105], v[80:95]
	v_max_f32_e32 v181, v173, v173
	v_mfma_f32_32x32x16_bf16 v[64:79], v[200:203], v[106:109], v[64:79]
	v_mfma_f32_32x32x16_bf16 v[80:95], v[188:191], v[98:101], v[80:95]
	v_mfma_f32_32x32x16_bf16 v[64:79], v[184:187], v[102:105], v[64:79]
	s_nop 10
	v_max_f32_e32 v174, v81, v81
	v_max_f32_e32 v180, v80, v80
	v_max_f32_e32 v174, v180, v174
	v_max3_f32 v174, v174, v82, v83
	v_max3_f32 v174, v174, v84, v85
	v_max3_f32 v174, v174, v86, v87
	v_max3_f32 v174, v174, v88, v89
	v_mfma_f32_32x32x16_bf16 v[64:79], v[192:195], v[98:101], v[64:79]
	v_max3_f32 v174, v174, v90, v91
	v_max3_f32 v174, v174, v92, v93
	v_max3_f32 v174, v174, v94, v95
	s_nop 8
	v_max3_f32 v174, v174, v64, v65
	v_max3_f32 v174, v174, v66, v67
	v_max3_f32 v174, v174, v68, v69
	v_max3_f32 v174, v174, v70, v71
	v_max3_f32 v174, v174, v72, v73
	v_max3_f32 v174, v174, v74, v75
	v_max3_f32 v174, v174, v76, v77
	v_max3_f32 v174, v174, v78, v79
	v_mov_b32_e32 v180, v174
	s_nop 1
	v_permlane32_swap_b32_e32 v174, v180
	v_max_f32_e32 v180, v180, v180
	v_max_f32_e32 v174, v174, v174
	v_max_f32_e32 v174, v174, v180
	v_sub_f32_e32 v180, v174, v173
	v_max_f32_e32 v174, v181, v174
	v_sub_f32_e32 v181, v173, v174
	v_mul_f32_e32 v181, 0x3dd53b94, v181
	v_exp_f32_e32 v181, v181
	v_cmp_ge_f32_e32 vcc, s33, v180
	s_cmp_eq_u64 vcc, exec
	s_cselect_b64 s[38:39], -1, 0
	v_cndmask_b32_e64 v180, v181, 1.0, s[38:39]
	v_cmp_gt_f32_e32 vcc, 1.0, v180
	s_cbranch_vccz .LBB0_1005
	s_and_saveexec_b64 s[0:1], s[36:37]
	ds_write_b32 v171, v180 offset:51328
	s_or_b64 exec, exec, s[0:1]
	s_waitcnt lgkmcnt(0)
	v_add_u32_e32 v181, v159, v96
	ds_read_b128 v[182:185], v181 offset:51424
	ds_read_b128 v[186:189], v181 offset:51392
	ds_read_b128 v[190:193], v181 offset:51360
	ds_read_b128 v[194:197], v181 offset:51328
	s_waitcnt lgkmcnt(3)
	v_pk_mul_f32 v[12:13], v[12:13], v[182:183]
	s_waitcnt lgkmcnt(2)
	v_pk_mul_f32 v[8:9], v[8:9], v[186:187]
	s_waitcnt lgkmcnt(1)
	v_pk_mul_f32 v[4:5], v[4:5], v[190:191]
	v_pk_mul_f32 v[14:15], v[14:15], v[184:185]
	v_pk_mul_f32 v[10:11], v[10:11], v[188:189]
	v_pk_mul_f32 v[6:7], v[6:7], v[192:193]
	s_waitcnt lgkmcnt(0)
	v_pk_mul_f32 v[2:3], v[2:3], v[196:197]
	v_pk_mul_f32 v[0:1], v[0:1], v[194:195]
	v_pk_mul_f32 v[60:61], v[60:61], v[182:183]
	v_pk_mul_f32 v[56:57], v[56:57], v[186:187]
	v_pk_mul_f32 v[52:53], v[52:53], v[190:191]
	v_pk_mul_f32 v[62:63], v[62:63], v[184:185]
	v_pk_mul_f32 v[58:59], v[58:59], v[188:189]
	v_pk_mul_f32 v[54:55], v[54:55], v[192:193]
	v_pk_mul_f32 v[50:51], v[50:51], v[196:197]
	v_pk_mul_f32 v[48:49], v[48:49], v[194:195]
	v_pk_mul_f32 v[44:45], v[44:45], v[182:183]
	v_pk_mul_f32 v[40:41], v[40:41], v[186:187]
	v_pk_mul_f32 v[36:37], v[36:37], v[190:191]
	v_pk_mul_f32 v[46:47], v[46:47], v[184:185]
	v_pk_mul_f32 v[42:43], v[42:43], v[188:189]
	v_pk_mul_f32 v[38:39], v[38:39], v[192:193]
	v_pk_mul_f32 v[34:35], v[34:35], v[196:197]
	v_pk_mul_f32 v[32:33], v[32:33], v[194:195]
	v_pk_mul_f32 v[28:29], v[28:29], v[182:183]
	v_pk_mul_f32 v[24:25], v[24:25], v[186:187]
	v_pk_mul_f32 v[20:21], v[20:21], v[190:191]
	v_pk_mul_f32 v[30:31], v[30:31], v[184:185]
	v_pk_mul_f32 v[26:27], v[26:27], v[188:189]
	v_pk_mul_f32 v[22:23], v[22:23], v[192:193]
	v_pk_mul_f32 v[18:19], v[18:19], v[196:197]
	v_pk_mul_f32 v[16:17], v[16:17], v[194:195]

; template <int OFF> __device__ __forceinline__ bf16x8 k_read(int kb) { bf16x8 r; asm volatile("ds_read_b128 %0, %1 offset:%2" : "=&v"(r) : "v"(kb), "i"(OFF) : "memory"); return r; }
; #define QK_STEP(D, X, Y, NEXT, N) do { K_WAIT(N, X, Y); \
;         p0 = __builtin_amdgcn_mfma_f32_32x32x16_bf16(X, qr[D], p0, 0, 0, 0); p1 = __builtin_amdgcn_mfma_f32_32x32x16_bf16(Y, qr[D], p1, 0, 0, 0); \
;         if constexpr ((NEXT) < 12) { X = k_read<(NEXT) * 32>(kb); Y = k_read<R1 + (NEXT) * 32>(kb); } } while (0)
; __device__ __forceinline__ void partialSM(f32x16& p0, f32x16& p1, float& m_reg, float& mn, float& alpha) {
;     constexpr float C = SCALE * 1.4426950408889634f;
;     float pmax = p0[0];
; #pragma unroll
;     for (int r = 1; r < 16; ++r) pmax = fmaxf(pmax, p0[r]);
; #pragma unroll
;     for (int r = 0; r < 16; ++r) pmax = fmaxf(pmax, p1[r]);
;     { auto rr = __builtin_amdgcn_permlane32_swap(__float_as_uint(pmax), __float_as_uint(pmax), false, false);
;       pmax = fmaxf(__uint_as_float(rr[0]), __uint_as_float(rr[1])); }
;     if (__builtin_expect(__all(pmax - m_reg <= THR / SCALE), 1)) { mn = m_reg; alpha = 1.f; }
;     else { mn = fmaxf(m_reg, pmax); alpha = __builtin_amdgcn_exp2f((m_reg - mn) * C); m_reg = mn; }
; __device__ __forceinline__ void qkt(f32x16& p0, f32x16& p1, const unsigned char* Ks, const bf16x8* qr, int r32, int hi) {
;     const int kb = (int)(uintptr_t)Ks + r32 * KPITCH + hi * 16;
;     constexpr int R1 = 32 * KPITCH;
;     p0 = f32x16{}; p1 = f32x16{};
;     bf16x8 a0 = k_read<0>(kb), a1 = k_read<R1>(kb), a2 = k_read<32>(kb), a3 = k_read<R1 + 32>(kb), a4 = k_read<64>(kb), a5 = k_read<R1 + 64>(kb);
;     ...
;     QK_STEP(0, a0, a1, 3, 4); QK_STEP(1, a2, a3, 4, 4); QK_STEP(2, a4, a5, 5, 4);
;     QK_STEP(3, a0, a1, 6, 4); QK_STEP(4, a2, a3, 7, 4); QK_STEP(5, a4, a5, 8, 4);
;     QK_STEP(6, a0, a1, 9, 4); QK_STEP(7, a2, a3, 10, 4); QK_STEP(8, a4, a5, 11, 4);
;     QK_STEP(9, a0, a1, 12, 4); QK_STEP(10, a2, a3, 12, 2); QK_STEP(11, a4, a5, 12, 0);
.LBB0_1007:
	s_cmp_lg_u32 0, -1
	s_cselect_b32 s0, 0, 0
	s_addk_i32 s0, 0x6400
	s_waitcnt lgkmcnt(0)
	s_barrier
	v_add_u32_e32 v164, s0, v178
	ds_read_b128 v[64:67], v164 offset:0
	ds_read_b128 v[68:71], v164 offset:0x3200
	s_waitcnt vmcnt(2)
	ds_read_b128 v[146:149], v164 offset:32
	s_waitcnt vmcnt(1)
	ds_read_b128 v[150:153], v164 offset:0x3220
	s_waitcnt vmcnt(0)
	ds_read_b128 v[154:157], v164 offset:64
	ds_read_b128 v[160:163], v164 offset:0x3240
	s_waitcnt lgkmcnt(4)
	v_mfma_f32_32x32x16_bf16 v[80:95], v[64:67], v[142:145], 0
	v_mfma_f32_32x32x16_bf16 v[64:79], v[68:71], v[142:145], 0
	ds_read_b128 v[142:145], v164 offset:0x60
	ds_read_b128 v[176:179], v164 offset:0x3260
	s_waitcnt lgkmcnt(4)
	v_mfma_f32_32x32x16_bf16 v[80:95], v[146:149], v[138:141], v[80:95]
	v_mfma_f32_32x32x16_bf16 v[64:79], v[150:153], v[138:141], v[64:79]
	ds_read_b128 v[138:141], v164 offset:0x80
	ds_read_b128 v[146:149], v164 offset:0x3280
	s_waitcnt lgkmcnt(4)
	v_mfma_f32_32x32x16_bf16 v[80:95], v[154:157], v[134:137], v[80:95]
	v_mfma_f32_32x32x16_bf16 v[64:79], v[160:163], v[134:137], v[64:79]
	ds_read_b128 v[134:137], v164 offset:0xa0
	ds_read_b128 v[150:153], v164 offset:0x32a0
	s_waitcnt lgkmcnt(4)
	v_mfma_f32_32x32x16_bf16 v[80:95], v[142:145], v[130:133], v[80:95]
	v_mfma_f32_32x32x16_bf16 v[64:79], v[176:179], v[130:133], v[64:79]
	ds_read_b128 v[130:133], v164 offset:0xc0
	ds_read_b128 v[142:145], v164 offset:0x32c0
	s_waitcnt lgkmcnt(4)
	v_mfma_f32_32x32x16_bf16 v[80:95], v[138:141], v[126:129], v[80:95]
	v_mfma_f32_32x32x16_bf16 v[64:79], v[146:149], v[126:129], v[64:79]
	ds_read_b128 v[126:129], v164 offset:0xe0
	ds_read_b128 v[138:141], v164 offset:0x32e0
	s_waitcnt lgkmcnt(4)
	v_mfma_f32_32x32x16_bf16 v[80:95], v[134:137], v[122:125], v[80:95]
	v_mfma_f32_32x32x16_bf16 v[64:79], v[150:153], v[122:125], v[64:79]
	ds_read_b128 v[122:125], v164 offset:0x100
	ds_read_b128 v[134:137], v164 offset:0x3300
	s_waitcnt lgkmcnt(4)
	v_mfma_f32_32x32x16_bf16 v[80:95], v[130:133], v[118:121], v[80:95]
	v_mfma_f32_32x32x16_bf16 v[64:79], v[142:145], v[118:121], v[64:79]
	ds_read_b128 v[118:121], v164 offset:0x120
	ds_read_b128 v[130:133], v164 offset:0x3320
	s_waitcnt lgkmcnt(4)
	v_mfma_f32_32x32x16_bf16 v[80:95], v[126:129], v[114:117], v[80:95]
	v_mfma_f32_32x32x16_bf16 v[64:79], v[138:141], v[114:117], v[64:79]
	ds_read_b128 v[114:117], v164 offset:0x140
	ds_read_b128 v[126:129], v164 offset:0x3340
	s_waitcnt lgkmcnt(4)
	v_mfma_f32_32x32x16_bf16 v[80:95], v[122:125], v[110:113], v[80:95]
	v_mfma_f32_32x32x16_bf16 v[64:79], v[134:137], v[110:113], v[64:79]
	ds_read_b128 v[110:113], v164 offset:0x160
	ds_read_b128 v[122:125], v164 offset:0x3360
	s_waitcnt lgkmcnt(4)
	s_waitcnt lgkmcnt(2)
	s_waitcnt lgkmcnt(0)
	v_mfma_f32_32x32x16_bf16 v[80:95], v[118:121], v[106:109], v[80:95]
	v_mfma_f32_32x32x16_bf16 v[80:95], v[114:117], v[102:105], v[80:95]
	v_mfma_f32_32x32x16_bf16 v[64:79], v[130:133], v[106:109], v[64:79]
	v_mfma_f32_32x32x16_bf16 v[80:95], v[110:113], v[98:101], v[80:95]
	v_mfma_f32_32x32x16_bf16 v[64:79], v[126:129], v[102:105], v[64:79]
	s_nop 10
	v_max_f32_e32 v106, v81, v81
	v_max_f32_e32 v107, v80, v80
	v_max_f32_e32 v106, v107, v106
	v_max3_f32 v102, v106, v82, v83
	v_max3_f32 v102, v102, v84, v85
	v_max3_f32 v102, v102, v86, v87
	v_max3_f32 v102, v102, v88, v89
	v_mfma_f32_32x32x16_bf16 v[64:79], v[122:125], v[98:101], v[64:79]
	v_max3_f32 v102, v102, v90, v91
	v_max3_f32 v102, v102, v92, v93
	v_max3_f32 v102, v102, v94, v95
	s_nop 8
	v_max3_f32 v98, v102, v64, v65
	v_max3_f32 v98, v98, v66, v67
	v_max3_f32 v98, v98, v68, v69
	v_max3_f32 v98, v98, v70, v71
	v_max3_f32 v98, v98, v72, v73
	v_max3_f32 v98, v98, v74, v75
	v_max3_f32 v98, v98, v76, v77
	v_max3_f32 v98, v98, v78, v79
	v_mov_b32_e32 v99, v98
	s_nop 1
	v_permlane32_swap_b32_e32 v98, v99
	v_max_f32_e32 v99, v99, v99
	v_max_f32_e32 v98, v98, v98
	v_max_f32_e32 v98, v98, v99
	v_max_f32_e32 v99, v173, v173
	v_max_f32_e32 v99, v99, v98
	v_sub_f32_e32 v100, v98, v173
	v_sub_f32_e32 v98, v173, v99
	v_mul_f32_e32 v98, 0x3dd53b94, v98
	v_exp_f32_e32 v98, v98
	v_cmp_ge_f32_e32 vcc, s33, v100
	s_cmp_eq_u64 vcc, exec
	s_cselect_b64 s[38:39], -1, 0
	v_cndmask_b32_e64 v98, v98, 1.0, s[38:39]
	v_cmp_gt_f32_e32 vcc, 1.0, v98
	s_cbranch_vccz .LBB0_1011
	s_and_saveexec_b64 s[0:1], s[36:37]
	ds_write_b32 v171, v98 offset:51328
	s_or_b64 exec, exec, s[0:1]
	s_waitcnt lgkmcnt(0)
	v_add_u32_e32 v112, v159, v96
	ds_read_b128 v[100:103], v112 offset:51424
	ds_read_b128 v[104:107], v112 offset:51392
	ds_read_b128 v[108:111], v112 offset:51360
	ds_read_b128 v[112:115], v112 offset:51328
	s_waitcnt lgkmcnt(3)
	v_pk_mul_f32 v[12:13], v[12:13], v[100:101]
	s_waitcnt lgkmcnt(2)
	v_pk_mul_f32 v[8:9], v[8:9], v[104:105]
	s_waitcnt lgkmcnt(1)
	v_pk_mul_f32 v[4:5], v[4:5], v[108:109]
	v_pk_mul_f32 v[14:15], v[14:15], v[102:103]
	v_pk_mul_f32 v[10:11], v[10:11], v[106:107]
	v_pk_mul_f32 v[6:7], v[6:7], v[110:111]
	s_waitcnt lgkmcnt(0)
	v_pk_mul_f32 v[2:3], v[2:3], v[114:115]
	v_pk_mul_f32 v[0:1], v[0:1], v[112:113]
	v_pk_mul_f32 v[60:61], v[60:61], v[100:101]
	v_pk_mul_f32 v[56:57], v[56:57], v[104:105]
	v_pk_mul_f32 v[52:53], v[52:53], v[108:109]
	v_pk_mul_f32 v[62:63], v[62:63], v[102:103]
	v_pk_mul_f32 v[58:59], v[58:59], v[106:107]
	v_pk_mul_f32 v[54:55], v[54:55], v[110:111]
	v_pk_mul_f32 v[50:51], v[50:51], v[114:115]
	v_pk_mul_f32 v[48:49], v[48:49], v[112:113]
	v_pk_mul_f32 v[44:45], v[44:45], v[100:101]
	v_pk_mul_f32 v[40:41], v[40:41], v[104:105]
	v_pk_mul_f32 v[36:37], v[36:37], v[108:109]
	v_pk_mul_f32 v[46:47], v[46:47], v[102:103]
	v_pk_mul_f32 v[42:43], v[42:43], v[106:107]
	v_pk_mul_f32 v[38:39], v[38:39], v[110:111]
	v_pk_mul_f32 v[34:35], v[34:35], v[114:115]
	v_pk_mul_f32 v[32:33], v[32:33], v[112:113]
	v_pk_mul_f32 v[28:29], v[28:29], v[100:101]
	v_pk_mul_f32 v[24:25], v[24:25], v[104:105]
	v_pk_mul_f32 v[20:21], v[20:21], v[108:109]
	v_pk_mul_f32 v[30:31], v[30:31], v[102:103]
	v_pk_mul_f32 v[26:27], v[26:27], v[106:107]
	v_pk_mul_f32 v[22:23], v[22:23], v[110:111]
	v_pk_mul_f32 v[18:19], v[18:19], v[114:115]
	v_pk_mul_f32 v[16:17], v[16:17], v[112:113]
